# grid barriers: flat release + arrivals with 8,16,24 still missing start an early L2 write-back
# baseline (speedup 1.0000x reference)
; __device__ __forceinline__ unsigned xb_ld(unsigned* p)              { return __hip_atomic_load(p, __ATOMIC_RELAXED, __HIP_MEMORY_SCOPE_AGENT); }
; __device__ __forceinline__ unsigned xb_add(unsigned* p, unsigned v) { return __hip_atomic_fetch_add(p, v, __ATOMIC_RELAXED, __HIP_MEMORY_SCOPE_AGENT); }
; #define XB_SPIN(cond, bar) do { unsigned _sp = 0; while (cond) { __builtin_amdgcn_s_sleep(1); \
;     if ((++_sp & 255u) == 0u) { if (xb_ld(&(bar)[XB_TMO])) break; if (_sp > XB_SPIN_CAP) { atomicAdd(&(bar)[XB_TMO], 1u); break; } } } } while (0)
; __device__ __forceinline__ void xcd_barrier(const XcdBarrier& b, const int tid) {
;     ...
;         const unsigned old = xb_add(&bar[XB_XSUB(b.x)], 1u);
;         const unsigned gen = old / nloc;
;         if (old + 1u == (gen + 1u) * nloc) {
;             __builtin_amdgcn_fence(__ATOMIC_RELEASE, "agent");
;             asm volatile("s_waitcnt vmcnt(0)" ::: "memory");
;             const unsigned og = xb_add(&bar[XB_TOP], 1u);
;             const unsigned tg = og / nx;
;             if (og + 1u == (tg + 1u) * nx) xb_add(&bar[XB_TOPGEN], 1u);
;             else XB_SPIN(xb_ld(&bar[XB_TOPGEN]) == tg, bar);
.LBB0_79:
	s_or_b64 exec, exec, s[16:17]
	v_cvt_f32_u32_e32 v4, v2
	s_waitcnt vmcnt(0)
	v_readfirstlane_b32 s12, v3
	v_sub_u32_e32 v3, 0, v2
	v_rcp_iflag_f32_e32 v4, v4
	v_add_u32_e32 v5, s12, v1
	v_mul_f32_e32 v4, 0x4f7ffffe, v4
	v_cvt_u32_f32_e32 v4, v4
	v_mul_lo_u32 v1, v3, v4
	v_mul_hi_u32 v1, v4, v1
	v_add_u32_e32 v1, v4, v1
	v_mul_hi_u32 v1, v5, v1
	v_mul_lo_u32 v3, v1, v2
	v_sub_u32_e32 v3, v5, v3
	v_add_u32_e32 v4, 1, v1
	v_cmp_ge_u32_e32 vcc, v3, v2
	s_nop 1
	v_cndmask_b32_e32 v1, v1, v4, vcc
	v_sub_u32_e32 v4, v3, v2
	v_cndmask_b32_e32 v3, v3, v4, vcc
	v_add_u32_e32 v4, 1, v1
	v_cmp_ge_u32_e32 vcc, v3, v2
	v_add_u32_e32 v3, 1, v5
	s_nop 0
	v_cndmask_b32_e32 v1, v1, v4, vcc
	v_mul_lo_u32 v4, v2, v1
	v_add_u32_e32 v2, v4, v2
	s_waitcnt lgkmcnt(0)
	v_add_u32_e32 v4, 1, v1
	v_mul_lo_u32 v4, v4, v0
	v_mov_b32_e32 v5, 0x3000
	v_cmp_ne_u32_e32 vcc, v3, v2
	s_cbranch_vccnz .Lgb0_nl
	buffer_wbl2 sc1
	s_waitcnt vmcnt(0) lgkmcnt(0)
	v_mov_b32_e32 v2, 1
	global_atomic_add v5, v2, s[26:27] offset:1024
	s_cmpk_lg_i32 s3, 0x100
	s_cbranch_scc1 .Lgb0_wait
	s_cmpk_ge_i32 s2, 0xa0
	s_cbranch_scc1 .Lgb0_out
	s_branch .Lgb0_wait

; __device__ __forceinline__ unsigned xb_ld(unsigned* p)              { return __hip_atomic_load(p, __ATOMIC_RELAXED, __HIP_MEMORY_SCOPE_AGENT); }
; #define XB_SPIN(cond, bar) do { unsigned _sp = 0; while (cond) { __builtin_amdgcn_s_sleep(1); \
;     if ((++_sp & 255u) == 0u) { if (xb_ld(&(bar)[XB_TMO])) break; if (_sp > XB_SPIN_CAP) { atomicAdd(&(bar)[XB_TMO], 1u); break; } } } } while (0)
; __device__ __forceinline__ void xcd_barrier(const XcdBarrier& b, const int tid) {
;     ...
;         } else {
;             XB_SPIN(xb_ld(&bar[XB_XGEN(b.x)]) == gen, bar);
;             __builtin_amdgcn_fence(__ATOMIC_ACQUIRE, "agent");
;             asm volatile("s_waitcnt vmcnt(0)" ::: "memory");
.Lgb0_spin0:
	v_sub_u32_e32 v2, v2, v3
	v_and_b32_e32 v2, 7, v2
	v_cmp_eq_u32_e32 vcc, 0, v2
	s_cbranch_vccz .Lgb0_wait
	buffer_wbl2 sc1

; __device__ __forceinline__ unsigned xb_ld(unsigned* p)              { return __hip_atomic_load(p, __ATOMIC_RELAXED, __HIP_MEMORY_SCOPE_AGENT); }
; __device__ __forceinline__ unsigned xb_add(unsigned* p, unsigned v) { return __hip_atomic_fetch_add(p, v, __ATOMIC_RELAXED, __HIP_MEMORY_SCOPE_AGENT); }
; #define XB_SPIN(cond, bar) do { unsigned _sp = 0; while (cond) { __builtin_amdgcn_s_sleep(1); \
;     if ((++_sp & 255u) == 0u) { if (xb_ld(&(bar)[XB_TMO])) break; if (_sp > XB_SPIN_CAP) { atomicAdd(&(bar)[XB_TMO], 1u); break; } } } } while (0)
; __device__ __forceinline__ void xcd_barrier(const XcdBarrier& b, const int tid) {
;     ...
;         const unsigned old = xb_add(&bar[XB_XSUB(b.x)], 1u);
;         const unsigned gen = old / nloc;
;         if (old + 1u == (gen + 1u) * nloc) {
;             __builtin_amdgcn_fence(__ATOMIC_RELEASE, "agent");
;             asm volatile("s_waitcnt vmcnt(0)" ::: "memory");
;             const unsigned og = xb_add(&bar[XB_TOP], 1u);
;             const unsigned tg = og / nx;
;             if (og + 1u == (tg + 1u) * nx) xb_add(&bar[XB_TOPGEN], 1u);
;             else XB_SPIN(xb_ld(&bar[XB_TOPGEN]) == tg, bar);
.LBB0_169:
	s_or_b64 exec, exec, s[22:23]
	v_cvt_f32_u32_e32 v4, v2
	s_waitcnt vmcnt(0)
	v_readfirstlane_b32 s20, v3
	v_sub_u32_e32 v3, 0, v2
	v_rcp_iflag_f32_e32 v4, v4
	v_add_u32_e32 v5, s20, v1
	v_mul_f32_e32 v4, 0x4f7ffffe, v4
	v_cvt_u32_f32_e32 v4, v4
	v_mul_lo_u32 v1, v3, v4
	v_mul_hi_u32 v1, v4, v1
	v_add_u32_e32 v1, v4, v1
	v_mul_hi_u32 v1, v5, v1
	v_mul_lo_u32 v3, v1, v2
	v_sub_u32_e32 v3, v5, v3
	v_add_u32_e32 v4, 1, v1
	v_cmp_ge_u32_e32 vcc, v3, v2
	s_nop 1
	v_cndmask_b32_e32 v1, v1, v4, vcc
	v_sub_u32_e32 v4, v3, v2
	v_cndmask_b32_e32 v3, v3, v4, vcc
	v_add_u32_e32 v4, 1, v1
	v_cmp_ge_u32_e32 vcc, v3, v2
	v_add_u32_e32 v3, 1, v5
	s_nop 0
	v_cndmask_b32_e32 v1, v1, v4, vcc
	v_mul_lo_u32 v4, v2, v1
	v_add_u32_e32 v2, v4, v2
	s_waitcnt lgkmcnt(0)
	v_add_u32_e32 v4, 1, v1
	v_mul_lo_u32 v4, v4, v0
	v_mov_b32_e32 v5, 0x3000
	v_cmp_ne_u32_e32 vcc, v3, v2
	s_cbranch_vccnz .Lgb1_nl
	buffer_wbl2 sc1
	s_waitcnt vmcnt(0) lgkmcnt(0)
	v_mov_b32_e32 v2, 1
	global_atomic_add v5, v2, s[26:27] offset:1024
	s_branch .Lgb1_wait

; __device__ __forceinline__ unsigned xb_ld(unsigned* p)              { return __hip_atomic_load(p, __ATOMIC_RELAXED, __HIP_MEMORY_SCOPE_AGENT); }
; __device__ __forceinline__ unsigned xb_add(unsigned* p, unsigned v) { return __hip_atomic_fetch_add(p, v, __ATOMIC_RELAXED, __HIP_MEMORY_SCOPE_AGENT); }
; #define XB_SPIN(cond, bar) do { unsigned _sp = 0; while (cond) { __builtin_amdgcn_s_sleep(1); \
;     if ((++_sp & 255u) == 0u) { if (xb_ld(&(bar)[XB_TMO])) break; if (_sp > XB_SPIN_CAP) { atomicAdd(&(bar)[XB_TMO], 1u); break; } } } } while (0)
; __device__ __forceinline__ void xcd_barrier(const XcdBarrier& b, const int tid) {
;     ...
;         const unsigned old = xb_add(&bar[XB_XSUB(b.x)], 1u);
;         const unsigned gen = old / nloc;
;         if (old + 1u == (gen + 1u) * nloc) {
;             __builtin_amdgcn_fence(__ATOMIC_RELEASE, "agent");
;             asm volatile("s_waitcnt vmcnt(0)" ::: "memory");
;             const unsigned og = xb_add(&bar[XB_TOP], 1u);
;             const unsigned tg = og / nx;
;             if (og + 1u == (tg + 1u) * nx) xb_add(&bar[XB_TOPGEN], 1u);
;             else XB_SPIN(xb_ld(&bar[XB_TOPGEN]) == tg, bar);
.LBB0_433:
	s_or_b64 exec, exec, s[12:13]
	v_cvt_f32_u32_e32 v4, v2
	s_waitcnt vmcnt(0)
	v_readfirstlane_b32 s6, v3
	v_sub_u32_e32 v3, 0, v2
	v_rcp_iflag_f32_e32 v4, v4
	v_add_u32_e32 v5, s6, v1
	v_mul_f32_e32 v4, 0x4f7ffffe, v4
	v_cvt_u32_f32_e32 v4, v4
	v_mul_lo_u32 v1, v3, v4
	v_mul_hi_u32 v1, v4, v1
	v_add_u32_e32 v1, v4, v1
	v_mul_hi_u32 v1, v5, v1
	v_mul_lo_u32 v3, v1, v2
	v_sub_u32_e32 v3, v5, v3
	v_add_u32_e32 v4, 1, v1
	v_cmp_ge_u32_e32 vcc, v3, v2
	s_nop 1
	v_cndmask_b32_e32 v1, v1, v4, vcc
	v_sub_u32_e32 v4, v3, v2
	v_cndmask_b32_e32 v3, v3, v4, vcc
	v_add_u32_e32 v4, 1, v1
	v_cmp_ge_u32_e32 vcc, v3, v2
	v_add_u32_e32 v3, 1, v5
	s_nop 0
	v_cndmask_b32_e32 v1, v1, v4, vcc
	v_mul_lo_u32 v4, v2, v1
	v_add_u32_e32 v2, v4, v2
	s_waitcnt lgkmcnt(0)
	v_add_u32_e32 v4, 1, v1
	v_mul_lo_u32 v4, v4, v0
	v_mov_b32_e32 v5, 0x3000
	v_cmp_ne_u32_e32 vcc, v3, v2
	s_cbranch_vccnz .Lgb2_nl
	buffer_wbl2 sc1
	s_waitcnt vmcnt(0) lgkmcnt(0)
	v_mov_b32_e32 v2, 1
	global_atomic_add v5, v2, s[26:27] offset:1024
	s_branch .Lgb2_wait

; __device__ __forceinline__ unsigned xb_ld(unsigned* p)              { return __hip_atomic_load(p, __ATOMIC_RELAXED, __HIP_MEMORY_SCOPE_AGENT); }
; __device__ __forceinline__ unsigned xb_add(unsigned* p, unsigned v) { return __hip_atomic_fetch_add(p, v, __ATOMIC_RELAXED, __HIP_MEMORY_SCOPE_AGENT); }
; #define XB_SPIN(cond, bar) do { unsigned _sp = 0; while (cond) { __builtin_amdgcn_s_sleep(1); \
;     if ((++_sp & 255u) == 0u) { if (xb_ld(&(bar)[XB_TMO])) break; if (_sp > XB_SPIN_CAP) { atomicAdd(&(bar)[XB_TMO], 1u); break; } } } } while (0)
; __device__ __forceinline__ void xcd_barrier(const XcdBarrier& b, const int tid) {
;     ...
;         const unsigned old = xb_add(&bar[XB_XSUB(b.x)], 1u);
;         const unsigned gen = old / nloc;
;         if (old + 1u == (gen + 1u) * nloc) {
;             __builtin_amdgcn_fence(__ATOMIC_RELEASE, "agent");
;             asm volatile("s_waitcnt vmcnt(0)" ::: "memory");
;             const unsigned og = xb_add(&bar[XB_TOP], 1u);
;             const unsigned tg = og / nx;
;             if (og + 1u == (tg + 1u) * nx) xb_add(&bar[XB_TOPGEN], 1u);
;             else XB_SPIN(xb_ld(&bar[XB_TOPGEN]) == tg, bar);
.LBB0_512:
	s_or_b64 exec, exec, s[8:9]
	v_cvt_f32_u32_e32 v4, v2
	s_waitcnt vmcnt(0)
	v_readfirstlane_b32 s6, v3
	v_sub_u32_e32 v3, 0, v2
	v_rcp_iflag_f32_e32 v4, v4
	v_add_u32_e32 v5, s6, v1
	v_mul_f32_e32 v4, 0x4f7ffffe, v4
	v_cvt_u32_f32_e32 v4, v4
	v_mul_lo_u32 v1, v3, v4
	v_mul_hi_u32 v1, v4, v1
	v_add_u32_e32 v1, v4, v1
	v_mul_hi_u32 v1, v5, v1
	v_mul_lo_u32 v3, v1, v2
	v_sub_u32_e32 v3, v5, v3
	v_add_u32_e32 v4, 1, v1
	v_cmp_ge_u32_e32 vcc, v3, v2
	s_nop 1
	v_cndmask_b32_e32 v1, v1, v4, vcc
	v_sub_u32_e32 v4, v3, v2
	v_cndmask_b32_e32 v3, v3, v4, vcc
	v_add_u32_e32 v4, 1, v1
	v_cmp_ge_u32_e32 vcc, v3, v2
	v_add_u32_e32 v3, 1, v5
	s_nop 0
	v_cndmask_b32_e32 v1, v1, v4, vcc
	v_mul_lo_u32 v4, v2, v1
	v_add_u32_e32 v2, v4, v2
	s_waitcnt lgkmcnt(0)
	v_add_u32_e32 v4, 1, v1
	v_mul_lo_u32 v4, v4, v0
	v_mov_b32_e32 v5, 0x3000
	v_cmp_ne_u32_e32 vcc, v3, v2
	s_cbranch_vccnz .Lgb3_nl
	buffer_wbl2 sc1
	s_waitcnt vmcnt(0) lgkmcnt(0)
	v_mov_b32_e32 v2, 1
	global_atomic_add v5, v2, s[26:27] offset:1024
	s_branch .Lgb3_wait

; __device__ __forceinline__ unsigned xb_ld(unsigned* p)              { return __hip_atomic_load(p, __ATOMIC_RELAXED, __HIP_MEMORY_SCOPE_AGENT); }
; __device__ __forceinline__ unsigned xb_add(unsigned* p, unsigned v) { return __hip_atomic_fetch_add(p, v, __ATOMIC_RELAXED, __HIP_MEMORY_SCOPE_AGENT); }
; #define XB_SPIN(cond, bar) do { unsigned _sp = 0; while (cond) { __builtin_amdgcn_s_sleep(1); \
;     if ((++_sp & 255u) == 0u) { if (xb_ld(&(bar)[XB_TMO])) break; if (_sp > XB_SPIN_CAP) { atomicAdd(&(bar)[XB_TMO], 1u); break; } } } } while (0)
; __device__ __forceinline__ void xcd_barrier(const XcdBarrier& b, const int tid) {
;     ...
;         const unsigned old = xb_add(&bar[XB_XSUB(b.x)], 1u);
;         const unsigned gen = old / nloc;
;         if (old + 1u == (gen + 1u) * nloc) {
;             __builtin_amdgcn_fence(__ATOMIC_RELEASE, "agent");
;             asm volatile("s_waitcnt vmcnt(0)" ::: "memory");
;             const unsigned og = xb_add(&bar[XB_TOP], 1u);
;             const unsigned tg = og / nx;
;             if (og + 1u == (tg + 1u) * nx) xb_add(&bar[XB_TOPGEN], 1u);
;             else XB_SPIN(xb_ld(&bar[XB_TOPGEN]) == tg, bar);
.LBB0_802:
	s_or_b64 exec, exec, s[10:11]
	v_cvt_f32_u32_e32 v4, v2
	s_waitcnt vmcnt(0)
	v_readfirstlane_b32 s8, v3
	v_sub_u32_e32 v3, 0, v2
	v_rcp_iflag_f32_e32 v4, v4
	v_add_u32_e32 v5, s8, v1
	v_mul_f32_e32 v4, 0x4f7ffffe, v4
	v_cvt_u32_f32_e32 v4, v4
	v_mul_lo_u32 v1, v3, v4
	v_mul_hi_u32 v1, v4, v1
	v_add_u32_e32 v1, v4, v1
	v_mul_hi_u32 v1, v5, v1
	v_mul_lo_u32 v3, v1, v2
	v_sub_u32_e32 v3, v5, v3
	v_add_u32_e32 v4, 1, v1
	v_cmp_ge_u32_e32 vcc, v3, v2
	s_nop 1
	v_cndmask_b32_e32 v1, v1, v4, vcc
	v_sub_u32_e32 v4, v3, v2
	v_cndmask_b32_e32 v3, v3, v4, vcc
	v_add_u32_e32 v4, 1, v1
	v_cmp_ge_u32_e32 vcc, v3, v2
	v_add_u32_e32 v3, 1, v5
	s_nop 0
	v_cndmask_b32_e32 v1, v1, v4, vcc
	v_mul_lo_u32 v4, v2, v1
	v_add_u32_e32 v2, v4, v2
	s_waitcnt lgkmcnt(0)
	v_add_u32_e32 v4, 1, v1
	v_mul_lo_u32 v4, v4, v0
	v_mov_b32_e32 v5, 0x3000
	v_cmp_ne_u32_e32 vcc, v3, v2
	s_cbranch_vccnz .Lgb5_nl
	buffer_wbl2 sc1
	s_waitcnt vmcnt(0) lgkmcnt(0)
	v_mov_b32_e32 v2, 1
	global_atomic_add v5, v2, s[26:27] offset:1024
	s_branch .Lgb5_wait
